# waitcnt cleanup: two counted lgkmcnt waits in the attention trip that were immediately followed by lgkmcnt(0) removed
# baseline (speedup 1.0000x reference)
.LBB0_1031:
	s_waitcnt lgkmcnt(0)
	s_mov_b64 s[42:43], 0
	v_mfma_f32_32x32x64_f8f6f4 v[50:65], v[146:153], v[66:73], v[50:65]
	v_mfma_f32_32x32x64_f8f6f4 v[34:49], v[138:145], v[66:73], v[34:49]
	v_mfma_f32_32x32x64_f8f6f4 v[18:33], v[130:137], v[66:73], v[18:33]
	v_mfma_f32_32x32x64_f8f6f4 v[2:17], v[122:129], v[66:73], v[2:17]

; #define V8_(a_, b_, c_, d_) ((unsigned)__builtin_amdgcn_cvt_pk_fp8_f32(c_, d_, __builtin_amdgcn_cvt_pk_fp8_f32(a_, b_, 0, false), true))
; #define PV_MMA() do { DSW4(4, va0, va1, va2, va3); o[0] = MMA8(CAT8(va0, va1), pf, o[0]); o[1] = MMA8(CAT8(va2, va3), pf, o[1]); \
;         DSW4(0, va4, va5, va6, va7); o[2] = MMA8(CAT8(va4, va5), pf, o[2]); o[3] = MMA8(CAT8(va6, va7), pf, o[3]); } while (0)
; __device__ __forceinline__ void attn_unit(LAS unsigned char* lds, const unsigned char* Q, const unsigned char* KV, const bf16_t* KPE, const float* CST, bf16_t* O, int b, int h, int qb, CvtState& cs) {
;     ...
;             for (int i = 0; i < 4; ++i) { pf[i] = (int)V8_(p0[4 * i], p0[4 * i + 1], p0[4 * i + 2], p0[4 * i + 3]); pf[4 + i] = (int)V8_(p1[4 * i], p1[4 * i + 1], p1[4 * i + 2], p1[4 * i + 3]); }
;             if (!lag) PV_MMA(); else pend = true;
.LBB0_1041:
	v_mov_b32_e32 v70, 0
	v_mov_b32_e32 v71, 0
	v_cvt_pk_fp8_f32 v70, v95, v67
	v_cvt_pk_fp8_f32 v71, v96, v221
	v_mov_b32_e32 v66, 0
	v_mov_b32_e32 v67, 0
	v_cvt_pk_fp8_f32 v70, v68, v69 op_sel:[0,0,1]
	v_cvt_pk_fp8_f32 v71, v72, v73 op_sel:[0,0,1]
	v_mov_b32_e32 v68, 0
	v_mov_b32_e32 v72, 0
	v_mov_b32_e32 v69, 0
	v_mov_b32_e32 v73, 0
	v_cvt_pk_fp8_f32 v66, v218, v219
	v_cvt_pk_fp8_f32 v67, v86, v220
	v_cvt_pk_fp8_f32 v68, v89, v90
	v_cvt_pk_fp8_f32 v72, v222, v223
	v_cvt_pk_fp8_f32 v69, v92, v94
	v_cvt_pk_fp8_f32 v73, v78, v224
	v_cvt_pk_fp8_f32 v66, v82, v83 op_sel:[0,0,1]
	v_cvt_pk_fp8_f32 v67, v85, v88 op_sel:[0,0,1]
	v_cvt_pk_fp8_f32 v68, v84, v87 op_sel:[0,0,1]
	v_cvt_pk_fp8_f32 v72, v97, v77 op_sel:[0,0,1]
	v_cvt_pk_fp8_f32 v69, v91, v93 op_sel:[0,0,1]
	v_cvt_pk_fp8_f32 v73, v79, v80 op_sel:[0,0,1]
	s_andn2_b64 vcc, exec, s[40:41]
	s_cbranch_vccnz .LBB0_1045
	s_waitcnt lgkmcnt(0)
	s_nop 0
	v_mfma_f32_32x32x64_f8f6f4 v[50:65], v[146:153], v[66:73], v[50:65]
	v_mfma_f32_32x32x64_f8f6f4 v[34:49], v[138:145], v[66:73], v[34:49]
	v_mfma_f32_32x32x64_f8f6f4 v[18:33], v[130:137], v[66:73], v[18:33]
	v_mfma_f32_32x32x64_f8f6f4 v[2:17], v[122:129], v[66:73], v[2:17]
	s_branch .LBB0_1046
